# speedup vs baseline: 1.0309x; 1.0309x over previous
_Z11prep_kernelPKfS0_S0_PDF16_PfPiS0_S1_:
	s_cmpk_lt_u32 s2, 0xc1
	s_mov_b64 s[4:5], -1
	s_cbranch_scc0 .LBB0_51
	s_cmpk_lg_i32 s2, 0xc0
	s_cbranch_scc0 .LBB0_11
	s_cmp_gt_u32 s2, 63
	s_cbranch_scc0 .LBB0_8
	s_load_dwordx4 s[4:7], s[0:1], 0x0
	s_load_dwordx2 s[28:29], s[0:1], 0x20
	s_sub_u32 s3, s2, 64
	v_readfirstlane_b32 s23, v0
	v_and_b32_e32 v1, 63, v0
	v_lshlrev_b32_e32 v100, 4, v1
	s_lshr_b32 s23, s23, 6
	s_lshr_b32 s27, s3, 1
	s_and_b32 s30, s3, 1
	s_lshl_b32 s8, s27, 12
	s_lshl_b32 s9, s23, 6
	s_add_u32 s8, s8, s9
	s_lshl_b32 s10, s23, 15
	s_lshl_b32 s9, s30, 10
	s_add_u32 s10, s10, s9
	s_waitcnt lgkmcnt(0)
	s_add_u32 s20, s4, s8
	s_addc_u32 s21, s5, 0
	s_add_u32 s24, s6, s10
	s_addc_u32 s25, s7, 0
	global_load_dwordx4 v[34:37], v100, s[24:25]
	global_load_dwordx4 v[38:41], v100, s[24:25] offset:2048
	s_add_u32 s24, s24, 0x1000
	s_addc_u32 s25, s25, 0
	s_load_dwordx8 s[32:39], s[20:21], 0x0
	s_load_dwordx8 s[40:47], s[20:21], 0x200
	s_load_dwordx8 s[48:55], s[20:21], 0x400
	s_load_dwordx8 s[56:63], s[20:21], 0x600
	s_load_dwordx8 s[64:71], s[20:21], 0x800
	s_load_dwordx8 s[72:79], s[20:21], 0xa00
	s_load_dwordx8 s[80:87], s[20:21], 0xc00
	s_load_dwordx8 s[88:95], s[20:21], 0xe00
	global_load_dwordx4 v[42:45], v100, s[24:25]
	global_load_dwordx4 v[46:49], v100, s[24:25] offset:2048
	s_add_u32 s24, s24, 0x1000
	s_addc_u32 s25, s25, 0
	global_load_dwordx4 v[50:53], v100, s[24:25]
	global_load_dwordx4 v[54:57], v100, s[24:25] offset:2048
	s_add_u32 s24, s24, 0x1000
	s_addc_u32 s25, s25, 0
	global_load_dwordx4 v[58:61], v100, s[24:25]
	global_load_dwordx4 v[62:65], v100, s[24:25] offset:2048
	s_add_u32 s24, s24, 0x1000
	s_addc_u32 s25, s25, 0
	global_load_dwordx4 v[66:69], v100, s[24:25]
	global_load_dwordx4 v[70:73], v100, s[24:25] offset:2048
	s_add_u32 s24, s24, 0x1000
	s_addc_u32 s25, s25, 0
	global_load_dwordx4 v[74:77], v100, s[24:25]
	global_load_dwordx4 v[78:81], v100, s[24:25] offset:2048
	s_add_u32 s24, s24, 0x1000
	s_addc_u32 s25, s25, 0
	global_load_dwordx4 v[82:85], v100, s[24:25]
	global_load_dwordx4 v[86:89], v100, s[24:25] offset:2048
	s_add_u32 s24, s24, 0x1000
	s_addc_u32 s25, s25, 0
	global_load_dwordx4 v[90:93], v100, s[24:25]
	global_load_dwordx4 v[94:97], v100, s[24:25] offset:2048
	v_mov_b64_e32 v[2:3], 0
	v_mov_b64_e32 v[4:5], 0
	v_mov_b64_e32 v[6:7], 0
	v_mov_b64_e32 v[8:9], 0
	v_mov_b64_e32 v[10:11], 0
	v_mov_b64_e32 v[12:13], 0
	v_mov_b64_e32 v[14:15], 0
	v_mov_b64_e32 v[16:17], 0
	v_mov_b64_e32 v[18:19], 0
	v_mov_b64_e32 v[20:21], 0
	v_mov_b64_e32 v[22:23], 0
	v_mov_b64_e32 v[24:25], 0
	v_mov_b64_e32 v[26:27], 0
	v_mov_b64_e32 v[28:29], 0
	v_mov_b64_e32 v[30:31], 0
	v_mov_b64_e32 v[32:33], 0
	s_waitcnt lgkmcnt(0)
	s_waitcnt vmcnt(15)
	v_pk_fma_f32 v[2:3], s[32:33], v[34:35], v[2:3] op_sel_hi:[0,1,1]
	v_pk_fma_f32 v[4:5], s[32:33], v[36:37], v[4:5] op_sel_hi:[0,1,1]
	v_pk_fma_f32 v[6:7], s[40:41], v[34:35], v[6:7] op_sel_hi:[0,1,1]
	v_pk_fma_f32 v[8:9], s[40:41], v[36:37], v[8:9] op_sel_hi:[0,1,1]
	v_pk_fma_f32 v[10:11], s[48:49], v[34:35], v[10:11] op_sel_hi:[0,1,1]
	v_pk_fma_f32 v[12:13], s[48:49], v[36:37], v[12:13] op_sel_hi:[0,1,1]
	v_pk_fma_f32 v[14:15], s[56:57], v[34:35], v[14:15] op_sel_hi:[0,1,1]
	v_pk_fma_f32 v[16:17], s[56:57], v[36:37], v[16:17] op_sel_hi:[0,1,1]
	v_pk_fma_f32 v[18:19], s[64:65], v[34:35], v[18:19] op_sel_hi:[0,1,1]
	v_pk_fma_f32 v[20:21], s[64:65], v[36:37], v[20:21] op_sel_hi:[0,1,1]
	v_pk_fma_f32 v[22:23], s[72:73], v[34:35], v[22:23] op_sel_hi:[0,1,1]
	v_pk_fma_f32 v[24:25], s[72:73], v[36:37], v[24:25] op_sel_hi:[0,1,1]
	v_pk_fma_f32 v[26:27], s[80:81], v[34:35], v[26:27] op_sel_hi:[0,1,1]
	v_pk_fma_f32 v[28:29], s[80:81], v[36:37], v[28:29] op_sel_hi:[0,1,1]
	v_pk_fma_f32 v[30:31], s[88:89], v[34:35], v[30:31] op_sel_hi:[0,1,1]
	v_pk_fma_f32 v[32:33], s[88:89], v[36:37], v[32:33] op_sel_hi:[0,1,1]
	s_waitcnt vmcnt(14)
	v_pk_fma_f32 v[2:3], s[32:33], v[38:39], v[2:3] op_sel:[1,0,0]
	v_pk_fma_f32 v[4:5], s[32:33], v[40:41], v[4:5] op_sel:[1,0,0]
	v_pk_fma_f32 v[6:7], s[40:41], v[38:39], v[6:7] op_sel:[1,0,0]
	v_pk_fma_f32 v[8:9], s[40:41], v[40:41], v[8:9] op_sel:[1,0,0]
	v_pk_fma_f32 v[10:11], s[48:49], v[38:39], v[10:11] op_sel:[1,0,0]
	v_pk_fma_f32 v[12:13], s[48:49], v[40:41], v[12:13] op_sel:[1,0,0]
	v_pk_fma_f32 v[14:15], s[56:57], v[38:39], v[14:15] op_sel:[1,0,0]
	v_pk_fma_f32 v[16:17], s[56:57], v[40:41], v[16:17] op_sel:[1,0,0]
	v_pk_fma_f32 v[18:19], s[64:65], v[38:39], v[18:19] op_sel:[1,0,0]
	v_pk_fma_f32 v[20:21], s[64:65], v[40:41], v[20:21] op_sel:[1,0,0]
	v_pk_fma_f32 v[22:23], s[72:73], v[38:39], v[22:23] op_sel:[1,0,0]
	v_pk_fma_f32 v[24:25], s[72:73], v[40:41], v[24:25] op_sel:[1,0,0]
	v_pk_fma_f32 v[26:27], s[80:81], v[38:39], v[26:27] op_sel:[1,0,0]
	v_pk_fma_f32 v[28:29], s[80:81], v[40:41], v[28:29] op_sel:[1,0,0]
	v_pk_fma_f32 v[30:31], s[88:89], v[38:39], v[30:31] op_sel:[1,0,0]
	v_pk_fma_f32 v[32:33], s[88:89], v[40:41], v[32:33] op_sel:[1,0,0]
	s_waitcnt vmcnt(13)
	v_pk_fma_f32 v[2:3], s[34:35], v[42:43], v[2:3] op_sel_hi:[0,1,1]
	v_pk_fma_f32 v[4:5], s[34:35], v[44:45], v[4:5] op_sel_hi:[0,1,1]
	v_pk_fma_f32 v[6:7], s[42:43], v[42:43], v[6:7] op_sel_hi:[0,1,1]
	v_pk_fma_f32 v[8:9], s[42:43], v[44:45], v[8:9] op_sel_hi:[0,1,1]
	v_pk_fma_f32 v[10:11], s[50:51], v[42:43], v[10:11] op_sel_hi:[0,1,1]
	v_pk_fma_f32 v[12:13], s[50:51], v[44:45], v[12:13] op_sel_hi:[0,1,1]
	v_pk_fma_f32 v[14:15], s[58:59], v[42:43], v[14:15] op_sel_hi:[0,1,1]
	v_pk_fma_f32 v[16:17], s[58:59], v[44:45], v[16:17] op_sel_hi:[0,1,1]
	v_pk_fma_f32 v[18:19], s[66:67], v[42:43], v[18:19] op_sel_hi:[0,1,1]
	v_pk_fma_f32 v[20:21], s[66:67], v[44:45], v[20:21] op_sel_hi:[0,1,1]
	v_pk_fma_f32 v[22:23], s[74:75], v[42:43], v[22:23] op_sel_hi:[0,1,1]
	v_pk_fma_f32 v[24:25], s[74:75], v[44:45], v[24:25] op_sel_hi:[0,1,1]
	v_pk_fma_f32 v[26:27], s[82:83], v[42:43], v[26:27] op_sel_hi:[0,1,1]
	v_pk_fma_f32 v[28:29], s[82:83], v[44:45], v[28:29] op_sel_hi:[0,1,1]
	v_pk_fma_f32 v[30:31], s[90:91], v[42:43], v[30:31] op_sel_hi:[0,1,1]
	v_pk_fma_f32 v[32:33], s[90:91], v[44:45], v[32:33] op_sel_hi:[0,1,1]
	s_waitcnt vmcnt(12)
	v_pk_fma_f32 v[2:3], s[34:35], v[46:47], v[2:3] op_sel:[1,0,0]
	v_pk_fma_f32 v[4:5], s[34:35], v[48:49], v[4:5] op_sel:[1,0,0]
	v_pk_fma_f32 v[6:7], s[42:43], v[46:47], v[6:7] op_sel:[1,0,0]
	v_pk_fma_f32 v[8:9], s[42:43], v[48:49], v[8:9] op_sel:[1,0,0]
	v_pk_fma_f32 v[10:11], s[50:51], v[46:47], v[10:11] op_sel:[1,0,0]
	v_pk_fma_f32 v[12:13], s[50:51], v[48:49], v[12:13] op_sel:[1,0,0]
	v_pk_fma_f32 v[14:15], s[58:59], v[46:47], v[14:15] op_sel:[1,0,0]
	v_pk_fma_f32 v[16:17], s[58:59], v[48:49], v[16:17] op_sel:[1,0,0]
	v_pk_fma_f32 v[18:19], s[66:67], v[46:47], v[18:19] op_sel:[1,0,0]
	v_pk_fma_f32 v[20:21], s[66:67], v[48:49], v[20:21] op_sel:[1,0,0]
	v_pk_fma_f32 v[22:23], s[74:75], v[46:47], v[22:23] op_sel:[1,0,0]
	v_pk_fma_f32 v[24:25], s[74:75], v[48:49], v[24:25] op_sel:[1,0,0]
	v_pk_fma_f32 v[26:27], s[82:83], v[46:47], v[26:27] op_sel:[1,0,0]
	v_pk_fma_f32 v[28:29], s[82:83], v[48:49], v[28:29] op_sel:[1,0,0]
	v_pk_fma_f32 v[30:31], s[90:91], v[46:47], v[30:31] op_sel:[1,0,0]
	v_pk_fma_f32 v[32:33], s[90:91], v[48:49], v[32:33] op_sel:[1,0,0]
	s_waitcnt vmcnt(11)
	v_pk_fma_f32 v[2:3], s[36:37], v[50:51], v[2:3] op_sel_hi:[0,1,1]
	v_pk_fma_f32 v[4:5], s[36:37], v[52:53], v[4:5] op_sel_hi:[0,1,1]
	v_pk_fma_f32 v[6:7], s[44:45], v[50:51], v[6:7] op_sel_hi:[0,1,1]
	v_pk_fma_f32 v[8:9], s[44:45], v[52:53], v[8:9] op_sel_hi:[0,1,1]
	v_pk_fma_f32 v[10:11], s[52:53], v[50:51], v[10:11] op_sel_hi:[0,1,1]
	v_pk_fma_f32 v[12:13], s[52:53], v[52:53], v[12:13] op_sel_hi:[0,1,1]
	v_pk_fma_f32 v[14:15], s[60:61], v[50:51], v[14:15] op_sel_hi:[0,1,1]
	v_pk_fma_f32 v[16:17], s[60:61], v[52:53], v[16:17] op_sel_hi:[0,1,1]
	v_pk_fma_f32 v[18:19], s[68:69], v[50:51], v[18:19] op_sel_hi:[0,1,1]
	v_pk_fma_f32 v[20:21], s[68:69], v[52:53], v[20:21] op_sel_hi:[0,1,1]
	v_pk_fma_f32 v[22:23], s[76:77], v[50:51], v[22:23] op_sel_hi:[0,1,1]
	v_pk_fma_f32 v[24:25], s[76:77], v[52:53], v[24:25] op_sel_hi:[0,1,1]
	v_pk_fma_f32 v[26:27], s[84:85], v[50:51], v[26:27] op_sel_hi:[0,1,1]
	v_pk_fma_f32 v[28:29], s[84:85], v[52:53], v[28:29] op_sel_hi:[0,1,1]
	v_pk_fma_f32 v[30:31], s[92:93], v[50:51], v[30:31] op_sel_hi:[0,1,1]
	v_pk_fma_f32 v[32:33], s[92:93], v[52:53], v[32:33] op_sel_hi:[0,1,1]
	s_waitcnt vmcnt(10)
	v_pk_fma_f32 v[2:3], s[36:37], v[54:55], v[2:3] op_sel:[1,0,0]
	v_pk_fma_f32 v[4:5], s[36:37], v[56:57], v[4:5] op_sel:[1,0,0]
	v_pk_fma_f32 v[6:7], s[44:45], v[54:55], v[6:7] op_sel:[1,0,0]
	v_pk_fma_f32 v[8:9], s[44:45], v[56:57], v[8:9] op_sel:[1,0,0]
	v_pk_fma_f32 v[10:11], s[52:53], v[54:55], v[10:11] op_sel:[1,0,0]
	v_pk_fma_f32 v[12:13], s[52:53], v[56:57], v[12:13] op_sel:[1,0,0]
	v_pk_fma_f32 v[14:15], s[60:61], v[54:55], v[14:15] op_sel:[1,0,0]
	v_pk_fma_f32 v[16:17], s[60:61], v[56:57], v[16:17] op_sel:[1,0,0]
	v_pk_fma_f32 v[18:19], s[68:69], v[54:55], v[18:19] op_sel:[1,0,0]
	v_pk_fma_f32 v[20:21], s[68:69], v[56:57], v[20:21] op_sel:[1,0,0]
	v_pk_fma_f32 v[22:23], s[76:77], v[54:55], v[22:23] op_sel:[1,0,0]
	v_pk_fma_f32 v[24:25], s[76:77], v[56:57], v[24:25] op_sel:[1,0,0]
	v_pk_fma_f32 v[26:27], s[84:85], v[54:55], v[26:27] op_sel:[1,0,0]
	v_pk_fma_f32 v[28:29], s[84:85], v[56:57], v[28:29] op_sel:[1,0,0]
	v_pk_fma_f32 v[30:31], s[92:93], v[54:55], v[30:31] op_sel:[1,0,0]
	v_pk_fma_f32 v[32:33], s[92:93], v[56:57], v[32:33] op_sel:[1,0,0]
	s_waitcnt vmcnt(9)
	v_pk_fma_f32 v[2:3], s[38:39], v[58:59], v[2:3] op_sel_hi:[0,1,1]
	v_pk_fma_f32 v[4:5], s[38:39], v[60:61], v[4:5] op_sel_hi:[0,1,1]
	v_pk_fma_f32 v[6:7], s[46:47], v[58:59], v[6:7] op_sel_hi:[0,1,1]
	v_pk_fma_f32 v[8:9], s[46:47], v[60:61], v[8:9] op_sel_hi:[0,1,1]
	v_pk_fma_f32 v[10:11], s[54:55], v[58:59], v[10:11] op_sel_hi:[0,1,1]
	v_pk_fma_f32 v[12:13], s[54:55], v[60:61], v[12:13] op_sel_hi:[0,1,1]
	v_pk_fma_f32 v[14:15], s[62:63], v[58:59], v[14:15] op_sel_hi:[0,1,1]
	v_pk_fma_f32 v[16:17], s[62:63], v[60:61], v[16:17] op_sel_hi:[0,1,1]
	v_pk_fma_f32 v[18:19], s[70:71], v[58:59], v[18:19] op_sel_hi:[0,1,1]
	v_pk_fma_f32 v[20:21], s[70:71], v[60:61], v[20:21] op_sel_hi:[0,1,1]
	v_pk_fma_f32 v[22:23], s[78:79], v[58:59], v[22:23] op_sel_hi:[0,1,1]
	v_pk_fma_f32 v[24:25], s[78:79], v[60:61], v[24:25] op_sel_hi:[0,1,1]
	v_pk_fma_f32 v[26:27], s[86:87], v[58:59], v[26:27] op_sel_hi:[0,1,1]
	v_pk_fma_f32 v[28:29], s[86:87], v[60:61], v[28:29] op_sel_hi:[0,1,1]
	v_pk_fma_f32 v[30:31], s[94:95], v[58:59], v[30:31] op_sel_hi:[0,1,1]
	v_pk_fma_f32 v[32:33], s[94:95], v[60:61], v[32:33] op_sel_hi:[0,1,1]
	s_waitcnt vmcnt(8)
	v_pk_fma_f32 v[2:3], s[38:39], v[62:63], v[2:3] op_sel:[1,0,0]
	v_pk_fma_f32 v[4:5], s[38:39], v[64:65], v[4:5] op_sel:[1,0,0]
	v_pk_fma_f32 v[6:7], s[46:47], v[62:63], v[6:7] op_sel:[1,0,0]
	v_pk_fma_f32 v[8:9], s[46:47], v[64:65], v[8:9] op_sel:[1,0,0]
	v_pk_fma_f32 v[10:11], s[54:55], v[62:63], v[10:11] op_sel:[1,0,0]
	v_pk_fma_f32 v[12:13], s[54:55], v[64:65], v[12:13] op_sel:[1,0,0]
	v_pk_fma_f32 v[14:15], s[62:63], v[62:63], v[14:15] op_sel:[1,0,0]
	v_pk_fma_f32 v[16:17], s[62:63], v[64:65], v[16:17] op_sel:[1,0,0]
	v_pk_fma_f32 v[18:19], s[70:71], v[62:63], v[18:19] op_sel:[1,0,0]
	v_pk_fma_f32 v[20:21], s[70:71], v[64:65], v[20:21] op_sel:[1,0,0]
	v_pk_fma_f32 v[22:23], s[78:79], v[62:63], v[22:23] op_sel:[1,0,0]
	v_pk_fma_f32 v[24:25], s[78:79], v[64:65], v[24:25] op_sel:[1,0,0]
	v_pk_fma_f32 v[26:27], s[86:87], v[62:63], v[26:27] op_sel:[1,0,0]
	v_pk_fma_f32 v[28:29], s[86:87], v[64:65], v[28:29] op_sel:[1,0,0]
	v_pk_fma_f32 v[30:31], s[94:95], v[62:63], v[30:31] op_sel:[1,0,0]
	v_pk_fma_f32 v[32:33], s[94:95], v[64:65], v[32:33] op_sel:[1,0,0]
	s_nop 0
	s_load_dwordx8 s[32:39], s[20:21], 0x20
	s_load_dwordx8 s[40:47], s[20:21], 0x220
	s_load_dwordx8 s[48:55], s[20:21], 0x420
	s_load_dwordx8 s[56:63], s[20:21], 0x620
	s_load_dwordx8 s[64:71], s[20:21], 0x820
	s_load_dwordx8 s[72:79], s[20:21], 0xa20
	s_load_dwordx8 s[80:87], s[20:21], 0xc20
	s_load_dwordx8 s[88:95], s[20:21], 0xe20
	s_waitcnt lgkmcnt(0)
	s_waitcnt vmcnt(7)
	v_pk_fma_f32 v[2:3], s[32:33], v[66:67], v[2:3] op_sel_hi:[0,1,1]
	v_pk_fma_f32 v[4:5], s[32:33], v[68:69], v[4:5] op_sel_hi:[0,1,1]
	v_pk_fma_f32 v[6:7], s[40:41], v[66:67], v[6:7] op_sel_hi:[0,1,1]
	v_pk_fma_f32 v[8:9], s[40:41], v[68:69], v[8:9] op_sel_hi:[0,1,1]
	v_pk_fma_f32 v[10:11], s[48:49], v[66:67], v[10:11] op_sel_hi:[0,1,1]
	v_pk_fma_f32 v[12:13], s[48:49], v[68:69], v[12:13] op_sel_hi:[0,1,1]
	v_pk_fma_f32 v[14:15], s[56:57], v[66:67], v[14:15] op_sel_hi:[0,1,1]
	v_pk_fma_f32 v[16:17], s[56:57], v[68:69], v[16:17] op_sel_hi:[0,1,1]
	v_pk_fma_f32 v[18:19], s[64:65], v[66:67], v[18:19] op_sel_hi:[0,1,1]
	v_pk_fma_f32 v[20:21], s[64:65], v[68:69], v[20:21] op_sel_hi:[0,1,1]
	v_pk_fma_f32 v[22:23], s[72:73], v[66:67], v[22:23] op_sel_hi:[0,1,1]
	v_pk_fma_f32 v[24:25], s[72:73], v[68:69], v[24:25] op_sel_hi:[0,1,1]
	v_pk_fma_f32 v[26:27], s[80:81], v[66:67], v[26:27] op_sel_hi:[0,1,1]
	v_pk_fma_f32 v[28:29], s[80:81], v[68:69], v[28:29] op_sel_hi:[0,1,1]
	v_pk_fma_f32 v[30:31], s[88:89], v[66:67], v[30:31] op_sel_hi:[0,1,1]
	v_pk_fma_f32 v[32:33], s[88:89], v[68:69], v[32:33] op_sel_hi:[0,1,1]
	s_waitcnt vmcnt(6)
	v_pk_fma_f32 v[2:3], s[32:33], v[70:71], v[2:3] op_sel:[1,0,0]
	v_pk_fma_f32 v[4:5], s[32:33], v[72:73], v[4:5] op_sel:[1,0,0]
	v_pk_fma_f32 v[6:7], s[40:41], v[70:71], v[6:7] op_sel:[1,0,0]
	v_pk_fma_f32 v[8:9], s[40:41], v[72:73], v[8:9] op_sel:[1,0,0]
	v_pk_fma_f32 v[10:11], s[48:49], v[70:71], v[10:11] op_sel:[1,0,0]
	v_pk_fma_f32 v[12:13], s[48:49], v[72:73], v[12:13] op_sel:[1,0,0]
	v_pk_fma_f32 v[14:15], s[56:57], v[70:71], v[14:15] op_sel:[1,0,0]
	v_pk_fma_f32 v[16:17], s[56:57], v[72:73], v[16:17] op_sel:[1,0,0]
	v_pk_fma_f32 v[18:19], s[64:65], v[70:71], v[18:19] op_sel:[1,0,0]
	v_pk_fma_f32 v[20:21], s[64:65], v[72:73], v[20:21] op_sel:[1,0,0]
	v_pk_fma_f32 v[22:23], s[72:73], v[70:71], v[22:23] op_sel:[1,0,0]
	v_pk_fma_f32 v[24:25], s[72:73], v[72:73], v[24:25] op_sel:[1,0,0]
	v_pk_fma_f32 v[26:27], s[80:81], v[70:71], v[26:27] op_sel:[1,0,0]
	v_pk_fma_f32 v[28:29], s[80:81], v[72:73], v[28:29] op_sel:[1,0,0]
	v_pk_fma_f32 v[30:31], s[88:89], v[70:71], v[30:31] op_sel:[1,0,0]
	v_pk_fma_f32 v[32:33], s[88:89], v[72:73], v[32:33] op_sel:[1,0,0]
	s_waitcnt vmcnt(5)
	v_pk_fma_f32 v[2:3], s[34:35], v[74:75], v[2:3] op_sel_hi:[0,1,1]
	v_pk_fma_f32 v[4:5], s[34:35], v[76:77], v[4:5] op_sel_hi:[0,1,1]
	v_pk_fma_f32 v[6:7], s[42:43], v[74:75], v[6:7] op_sel_hi:[0,1,1]
	v_pk_fma_f32 v[8:9], s[42:43], v[76:77], v[8:9] op_sel_hi:[0,1,1]
	v_pk_fma_f32 v[10:11], s[50:51], v[74:75], v[10:11] op_sel_hi:[0,1,1]
	v_pk_fma_f32 v[12:13], s[50:51], v[76:77], v[12:13] op_sel_hi:[0,1,1]
	v_pk_fma_f32 v[14:15], s[58:59], v[74:75], v[14:15] op_sel_hi:[0,1,1]
	v_pk_fma_f32 v[16:17], s[58:59], v[76:77], v[16:17] op_sel_hi:[0,1,1]
	v_pk_fma_f32 v[18:19], s[66:67], v[74:75], v[18:19] op_sel_hi:[0,1,1]
	v_pk_fma_f32 v[20:21], s[66:67], v[76:77], v[20:21] op_sel_hi:[0,1,1]
	v_pk_fma_f32 v[22:23], s[74:75], v[74:75], v[22:23] op_sel_hi:[0,1,1]
	v_pk_fma_f32 v[24:25], s[74:75], v[76:77], v[24:25] op_sel_hi:[0,1,1]
	v_pk_fma_f32 v[26:27], s[82:83], v[74:75], v[26:27] op_sel_hi:[0,1,1]
	v_pk_fma_f32 v[28:29], s[82:83], v[76:77], v[28:29] op_sel_hi:[0,1,1]
	v_pk_fma_f32 v[30:31], s[90:91], v[74:75], v[30:31] op_sel_hi:[0,1,1]
	v_pk_fma_f32 v[32:33], s[90:91], v[76:77], v[32:33] op_sel_hi:[0,1,1]
	s_waitcnt vmcnt(4)
	v_pk_fma_f32 v[2:3], s[34:35], v[78:79], v[2:3] op_sel:[1,0,0]
	v_pk_fma_f32 v[4:5], s[34:35], v[80:81], v[4:5] op_sel:[1,0,0]
	v_pk_fma_f32 v[6:7], s[42:43], v[78:79], v[6:7] op_sel:[1,0,0]
	v_pk_fma_f32 v[8:9], s[42:43], v[80:81], v[8:9] op_sel:[1,0,0]
	v_pk_fma_f32 v[10:11], s[50:51], v[78:79], v[10:11] op_sel:[1,0,0]
	v_pk_fma_f32 v[12:13], s[50:51], v[80:81], v[12:13] op_sel:[1,0,0]
	v_pk_fma_f32 v[14:15], s[58:59], v[78:79], v[14:15] op_sel:[1,0,0]
	v_pk_fma_f32 v[16:17], s[58:59], v[80:81], v[16:17] op_sel:[1,0,0]
	v_pk_fma_f32 v[18:19], s[66:67], v[78:79], v[18:19] op_sel:[1,0,0]
	v_pk_fma_f32 v[20:21], s[66:67], v[80:81], v[20:21] op_sel:[1,0,0]
	v_pk_fma_f32 v[22:23], s[74:75], v[78:79], v[22:23] op_sel:[1,0,0]
	v_pk_fma_f32 v[24:25], s[74:75], v[80:81], v[24:25] op_sel:[1,0,0]
	v_pk_fma_f32 v[26:27], s[82:83], v[78:79], v[26:27] op_sel:[1,0,0]
	v_pk_fma_f32 v[28:29], s[82:83], v[80:81], v[28:29] op_sel:[1,0,0]
	v_pk_fma_f32 v[30:31], s[90:91], v[78:79], v[30:31] op_sel:[1,0,0]
	v_pk_fma_f32 v[32:33], s[90:91], v[80:81], v[32:33] op_sel:[1,0,0]
	s_waitcnt vmcnt(3)
	v_pk_fma_f32 v[2:3], s[36:37], v[82:83], v[2:3] op_sel_hi:[0,1,1]
	v_pk_fma_f32 v[4:5], s[36:37], v[84:85], v[4:5] op_sel_hi:[0,1,1]
	v_pk_fma_f32 v[6:7], s[44:45], v[82:83], v[6:7] op_sel_hi:[0,1,1]
	v_pk_fma_f32 v[8:9], s[44:45], v[84:85], v[8:9] op_sel_hi:[0,1,1]
	v_pk_fma_f32 v[10:11], s[52:53], v[82:83], v[10:11] op_sel_hi:[0,1,1]
	v_pk_fma_f32 v[12:13], s[52:53], v[84:85], v[12:13] op_sel_hi:[0,1,1]
	v_pk_fma_f32 v[14:15], s[60:61], v[82:83], v[14:15] op_sel_hi:[0,1,1]
	v_pk_fma_f32 v[16:17], s[60:61], v[84:85], v[16:17] op_sel_hi:[0,1,1]
	v_pk_fma_f32 v[18:19], s[68:69], v[82:83], v[18:19] op_sel_hi:[0,1,1]
	v_pk_fma_f32 v[20:21], s[68:69], v[84:85], v[20:21] op_sel_hi:[0,1,1]
	v_pk_fma_f32 v[22:23], s[76:77], v[82:83], v[22:23] op_sel_hi:[0,1,1]
	v_pk_fma_f32 v[24:25], s[76:77], v[84:85], v[24:25] op_sel_hi:[0,1,1]
	v_pk_fma_f32 v[26:27], s[84:85], v[82:83], v[26:27] op_sel_hi:[0,1,1]
	v_pk_fma_f32 v[28:29], s[84:85], v[84:85], v[28:29] op_sel_hi:[0,1,1]
	v_pk_fma_f32 v[30:31], s[92:93], v[82:83], v[30:31] op_sel_hi:[0,1,1]
	v_pk_fma_f32 v[32:33], s[92:93], v[84:85], v[32:33] op_sel_hi:[0,1,1]
	s_waitcnt vmcnt(2)
	v_pk_fma_f32 v[2:3], s[36:37], v[86:87], v[2:3] op_sel:[1,0,0]
	v_pk_fma_f32 v[4:5], s[36:37], v[88:89], v[4:5] op_sel:[1,0,0]
	v_pk_fma_f32 v[6:7], s[44:45], v[86:87], v[6:7] op_sel:[1,0,0]
	v_pk_fma_f32 v[8:9], s[44:45], v[88:89], v[8:9] op_sel:[1,0,0]
	v_pk_fma_f32 v[10:11], s[52:53], v[86:87], v[10:11] op_sel:[1,0,0]
	v_pk_fma_f32 v[12:13], s[52:53], v[88:89], v[12:13] op_sel:[1,0,0]
	v_pk_fma_f32 v[14:15], s[60:61], v[86:87], v[14:15] op_sel:[1,0,0]
	v_pk_fma_f32 v[16:17], s[60:61], v[88:89], v[16:17] op_sel:[1,0,0]
	v_pk_fma_f32 v[18:19], s[68:69], v[86:87], v[18:19] op_sel:[1,0,0]
	v_pk_fma_f32 v[20:21], s[68:69], v[88:89], v[20:21] op_sel:[1,0,0]
	v_pk_fma_f32 v[22:23], s[76:77], v[86:87], v[22:23] op_sel:[1,0,0]
	v_pk_fma_f32 v[24:25], s[76:77], v[88:89], v[24:25] op_sel:[1,0,0]
	v_pk_fma_f32 v[26:27], s[84:85], v[86:87], v[26:27] op_sel:[1,0,0]
	v_pk_fma_f32 v[28:29], s[84:85], v[88:89], v[28:29] op_sel:[1,0,0]
	v_pk_fma_f32 v[30:31], s[92:93], v[86:87], v[30:31] op_sel:[1,0,0]
	v_pk_fma_f32 v[32:33], s[92:93], v[88:89], v[32:33] op_sel:[1,0,0]
	s_waitcnt vmcnt(1)
	v_pk_fma_f32 v[2:3], s[38:39], v[90:91], v[2:3] op_sel_hi:[0,1,1]
	v_pk_fma_f32 v[4:5], s[38:39], v[92:93], v[4:5] op_sel_hi:[0,1,1]
	v_pk_fma_f32 v[6:7], s[46:47], v[90:91], v[6:7] op_sel_hi:[0,1,1]
	v_pk_fma_f32 v[8:9], s[46:47], v[92:93], v[8:9] op_sel_hi:[0,1,1]
	v_pk_fma_f32 v[10:11], s[54:55], v[90:91], v[10:11] op_sel_hi:[0,1,1]
	v_pk_fma_f32 v[12:13], s[54:55], v[92:93], v[12:13] op_sel_hi:[0,1,1]
	v_pk_fma_f32 v[14:15], s[62:63], v[90:91], v[14:15] op_sel_hi:[0,1,1]
	v_pk_fma_f32 v[16:17], s[62:63], v[92:93], v[16:17] op_sel_hi:[0,1,1]
	v_pk_fma_f32 v[18:19], s[70:71], v[90:91], v[18:19] op_sel_hi:[0,1,1]
	v_pk_fma_f32 v[20:21], s[70:71], v[92:93], v[20:21] op_sel_hi:[0,1,1]
	v_pk_fma_f32 v[22:23], s[78:79], v[90:91], v[22:23] op_sel_hi:[0,1,1]
	v_pk_fma_f32 v[24:25], s[78:79], v[92:93], v[24:25] op_sel_hi:[0,1,1]
	v_pk_fma_f32 v[26:27], s[86:87], v[90:91], v[26:27] op_sel_hi:[0,1,1]
	v_pk_fma_f32 v[28:29], s[86:87], v[92:93], v[28:29] op_sel_hi:[0,1,1]
	v_pk_fma_f32 v[30:31], s[94:95], v[90:91], v[30:31] op_sel_hi:[0,1,1]
	v_pk_fma_f32 v[32:33], s[94:95], v[92:93], v[32:33] op_sel_hi:[0,1,1]
	s_waitcnt vmcnt(0)
	v_pk_fma_f32 v[2:3], s[38:39], v[94:95], v[2:3] op_sel:[1,0,0]
	v_pk_fma_f32 v[4:5], s[38:39], v[96:97], v[4:5] op_sel:[1,0,0]
	v_pk_fma_f32 v[6:7], s[46:47], v[94:95], v[6:7] op_sel:[1,0,0]
	v_pk_fma_f32 v[8:9], s[46:47], v[96:97], v[8:9] op_sel:[1,0,0]
	v_pk_fma_f32 v[10:11], s[54:55], v[94:95], v[10:11] op_sel:[1,0,0]
	v_pk_fma_f32 v[12:13], s[54:55], v[96:97], v[12:13] op_sel:[1,0,0]
	v_pk_fma_f32 v[14:15], s[62:63], v[94:95], v[14:15] op_sel:[1,0,0]
	v_pk_fma_f32 v[16:17], s[62:63], v[96:97], v[16:17] op_sel:[1,0,0]
	v_pk_fma_f32 v[18:19], s[70:71], v[94:95], v[18:19] op_sel:[1,0,0]
	v_pk_fma_f32 v[20:21], s[70:71], v[96:97], v[20:21] op_sel:[1,0,0]
	v_pk_fma_f32 v[22:23], s[78:79], v[94:95], v[22:23] op_sel:[1,0,0]
	v_pk_fma_f32 v[24:25], s[78:79], v[96:97], v[24:25] op_sel:[1,0,0]
	v_pk_fma_f32 v[26:27], s[86:87], v[94:95], v[26:27] op_sel:[1,0,0]
	v_pk_fma_f32 v[28:29], s[86:87], v[96:97], v[28:29] op_sel:[1,0,0]
	v_pk_fma_f32 v[30:31], s[94:95], v[94:95], v[30:31] op_sel:[1,0,0]
	v_pk_fma_f32 v[32:33], s[94:95], v[96:97], v[32:33] op_sel:[1,0,0]
	s_lshl_b32 s9, s23, 13
	v_add_u32_e32 v98, s9, v100
	ds_write_b128 v98, v[2:5] offset:0
	ds_write_b128 v98, v[6:9] offset:1024
	ds_write_b128 v98, v[10:13] offset:2048
	ds_write_b128 v98, v[14:17] offset:3072
	ds_write_b128 v98, v[18:21] offset:4096
	ds_write_b128 v98, v[22:25] offset:5120
	ds_write_b128 v98, v[26:29] offset:6144
	ds_write_b128 v98, v[30:33] offset:7168
	s_lshl_b32 s9, s23, 10
	v_add_u32_e32 v99, s9, v100
	s_waitcnt lgkmcnt(0)
	s_barrier
	ds_read_b128 v[34:37], v99 offset:0
	ds_read_b128 v[38:41], v99 offset:8192
	ds_read_b128 v[42:45], v99 offset:16384
	ds_read_b128 v[46:49], v99 offset:24576
	ds_read_b128 v[50:53], v99 offset:32768
	ds_read_b128 v[54:57], v99 offset:40960
	ds_read_b128 v[58:61], v99 offset:49152
	ds_read_b128 v[62:65], v99 offset:57344
	s_lshl_b32 s8, s27, 3
	s_add_u32 s8, s8, s23
	s_lshl_b32 s8, s8, 11
	s_lshl_b32 s9, s30, 10
	s_add_u32 s8, s8, s9
	s_add_u32 s28, s28, s8
	s_addc_u32 s29, s29, 0
	s_waitcnt lgkmcnt(6)
	v_pk_add_f32 v[34:35], v[34:35], v[38:39]
	v_pk_add_f32 v[36:37], v[36:37], v[40:41]
	s_waitcnt lgkmcnt(5)
	v_pk_add_f32 v[34:35], v[34:35], v[42:43]
	v_pk_add_f32 v[36:37], v[36:37], v[44:45]
	s_waitcnt lgkmcnt(4)
	v_pk_add_f32 v[34:35], v[34:35], v[46:47]
	v_pk_add_f32 v[36:37], v[36:37], v[48:49]
	s_waitcnt lgkmcnt(3)
	v_pk_add_f32 v[34:35], v[34:35], v[50:51]
	v_pk_add_f32 v[36:37], v[36:37], v[52:53]
	s_waitcnt lgkmcnt(2)
	v_pk_add_f32 v[34:35], v[34:35], v[54:55]
	v_pk_add_f32 v[36:37], v[36:37], v[56:57]
	s_waitcnt lgkmcnt(1)
	v_pk_add_f32 v[34:35], v[34:35], v[58:59]
	v_pk_add_f32 v[36:37], v[36:37], v[60:61]
	s_waitcnt lgkmcnt(0)
	v_pk_add_f32 v[34:35], v[34:35], v[62:63]
	v_pk_add_f32 v[36:37], v[36:37], v[64:65]
	global_store_dwordx4 v100, v[34:37], s[28:29]
